# v37: v36 + 32 more int-to-float converts ahead of the realign barrier
# baseline (speedup 1.0000x reference)
.LBB0_1508:
	s_add_u32 s42, s40, 0xfffe0080
	s_addc_u32 s43, s41, -1
	s_add_i32 s68, 0, 0x10000
	s_cmp_eq_u32 s67, 4
	s_cselect_b32 s43, s23, s43
	s_cselect_b32 s42, s29, s42
	v_add_u32_e32 v0, s68, v157
	s_cselect_b32 s45, s31, s66
	s_cselect_b32 s44, s30, s37
	s_add_i32 s70, 0, 0x14000
	ds_read_b128 v[82:85], v0
	ds_read_b128 v[86:89], v0 offset:1024
	ds_read_b128 v[90:93], v0 offset:2048
	ds_read_b128 v[94:97], v0 offset:3072
	v_add_u32_e32 v0, s70, v157
	ds_read_b128 v[160:163], v0
	ds_read_b128 v[164:167], v0 offset:1024
	ds_read_b128 v[168:171], v0 offset:2048
	ds_read_b128 v[172:175], v0 offset:3072
	v_mov_b32_e32 v0, v149
	ds_read_b128 v[176:179], v159
	ds_read_b128 v[180:183], v159 offset:1024
	ds_read_b128 v[184:187], v159 offset:2048
	ds_read_b128 v[188:191], v159 offset:3072
	ds_read_b128 v[192:195], v159 offset:4096
	ds_read_b128 v[196:199], v159 offset:5120
	ds_read_b128 v[200:203], v159 offset:6144
	ds_read_b128 v[204:207], v159 offset:7168
	s_add_i32 m0, s85, 0xc000
	s_nop 0
	global_load_lds_dwordx4 v0, s[40:41]
	v_mov_b32_e32 v0, v153
	s_add_i32 m0, s85, 0xe000
	s_nop 0
	global_load_lds_dwordx4 v0, s[40:41]
	s_waitcnt vmcnt(8)
	s_waitcnt lgkmcnt(0)
	s_barrier
	s_setprio 1
	s_waitcnt lgkmcnt(0)
	v_mfma_i32_16x16x64_i8 v[142:145], v[82:85], v[176:179], v[142:145]
	v_mfma_i32_16x16x64_i8 v[134:137], v[90:93], v[176:179], v[134:137]
	v_mfma_i32_16x16x64_i8 v[126:129], v[82:85], v[184:187], v[126:129]
	v_mfma_i32_16x16x64_i8 v[122:125], v[90:93], v[184:187], v[122:125]
	v_mfma_i32_16x16x64_i8 v[110:113], v[82:85], v[192:195], v[110:113]
	v_mfma_i32_16x16x64_i8 v[106:109], v[90:93], v[192:195], v[106:109]
	v_mfma_i32_16x16x64_i8 v[78:81], v[82:85], v[200:203], v[78:81]
	v_mfma_i32_16x16x64_i8 v[74:77], v[90:93], v[200:203], v[74:77]
	v_mfma_i32_16x16x64_i8 v[142:145], v[86:89], v[180:183], v[142:145]
	v_mfma_i32_16x16x64_i8 v[134:137], v[94:97], v[180:183], v[134:137]
	v_mfma_i32_16x16x64_i8 v[126:129], v[86:89], v[188:191], v[126:129]
	v_mfma_i32_16x16x64_i8 v[122:125], v[94:97], v[188:191], v[122:125]
	v_mfma_i32_16x16x64_i8 v[110:113], v[86:89], v[196:199], v[110:113]
	v_mfma_i32_16x16x64_i8 v[106:109], v[94:97], v[196:199], v[106:109]
	v_mfma_i32_16x16x64_i8 v[78:81], v[86:89], v[204:207], v[78:81]
	v_mfma_i32_16x16x64_i8 v[74:77], v[94:97], v[204:207], v[74:77]
	s_setprio 0
	s_setprio 1
	v_mfma_i32_16x16x64_i8 v[138:141], v[160:163], v[176:179], v[138:141]
	v_mfma_i32_16x16x64_i8 v[130:133], v[168:171], v[176:179], v[130:133]
	v_mfma_i32_16x16x64_i8 v[118:121], v[160:163], v[184:187], v[118:121]
	v_mfma_i32_16x16x64_i8 v[114:117], v[168:171], v[184:187], v[114:117]
	v_mfma_i32_16x16x64_i8 v[102:105], v[160:163], v[192:195], v[102:105]
	v_mfma_i32_16x16x64_i8 v[98:101], v[168:171], v[192:195], v[98:101]
	v_mfma_i32_16x16x64_i8 v[70:73], v[160:163], v[200:203], v[70:73]
	v_mfma_i32_16x16x64_i8 v[66:69], v[168:171], v[200:203], v[66:69]
	v_mfma_i32_16x16x64_i8 v[138:141], v[164:167], v[180:183], v[138:141]
	v_mfma_i32_16x16x64_i8 v[130:133], v[172:175], v[180:183], v[130:133]
	v_mfma_i32_16x16x64_i8 v[118:121], v[164:167], v[188:191], v[118:121]
	v_mfma_i32_16x16x64_i8 v[114:117], v[172:175], v[188:191], v[114:117]
	v_mfma_i32_16x16x64_i8 v[102:105], v[164:167], v[196:199], v[102:105]
	v_mfma_i32_16x16x64_i8 v[98:101], v[172:175], v[196:199], v[98:101]
	v_mfma_i32_16x16x64_i8 v[70:73], v[164:167], v[204:207], v[70:73]
	v_mfma_i32_16x16x64_i8 v[66:69], v[172:175], v[204:207], v[66:69]
	s_setprio 0
	s_barrier
	v_mov_b32_e32 v0, v151
	s_add_i32 s68, s68, s33
	ds_read_b128 v[176:179], v159 offset:16384
	ds_read_b128 v[180:183], v159 offset:17408
	ds_read_b128 v[184:187], v159 offset:18432
	ds_read_b128 v[188:191], v159 offset:19456
	ds_read_b128 v[192:195], v159 offset:20480
	ds_read_b128 v[196:199], v159 offset:21504
	ds_read_b128 v[200:203], v159 offset:22528
	ds_read_b128 v[204:207], v159 offset:23552
	s_mov_b32 m0, s68
	s_nop 0
	global_load_lds_dwordx4 v0, s[44:45]
	v_mov_b32_e32 v0, v155
	s_add_i32 m0, s68, 0x2000
	s_add_u32 s68, s44, 0x20000
	global_load_lds_dwordx4 v0, s[44:45]
	s_addc_u32 s69, s45, 0
	v_mov_b32_e32 v0, v151
	s_add_i32 s70, s70, s33
	s_mov_b32 m0, s70
	s_nop 0
	global_load_lds_dwordx4 v0, s[68:69]
	v_mov_b32_e32 v0, v155
	s_add_i32 m0, s70, 0x2000
	s_nop 0
	global_load_lds_dwordx4 v0, s[68:69]
	v_mov_b32_e32 v0, v149
	s_mov_b32 m0, s85
	s_nop 0
	global_load_lds_dwordx4 v0, s[42:43]
	v_mov_b32_e32 v0, v153
	s_mov_b32 m0, s56
	s_nop 0
	global_load_lds_dwordx4 v0, s[42:43]
	s_waitcnt vmcnt(8)
	s_waitcnt lgkmcnt(0)
	s_barrier
	s_setprio 1
	s_waitcnt lgkmcnt(0)
	v_mfma_i32_16x16x64_i8 v[62:65], v[82:85], v[176:179], v[62:65]
	v_mfma_i32_16x16x64_i8 v[58:61], v[90:93], v[176:179], v[58:61]
	v_mfma_i32_16x16x64_i8 v[46:49], v[82:85], v[184:187], v[46:49]
	v_mfma_i32_16x16x64_i8 v[42:45], v[90:93], v[184:187], v[42:45]
	v_mfma_i32_16x16x64_i8 v[30:33], v[82:85], v[192:195], v[30:33]
	v_mfma_i32_16x16x64_i8 v[26:29], v[90:93], v[192:195], v[26:29]
	v_mfma_i32_16x16x64_i8 v[14:17], v[82:85], v[200:203], v[14:17]
	v_mfma_i32_16x16x64_i8 v[10:13], v[90:93], v[200:203], v[10:13]
	v_mfma_i32_16x16x64_i8 v[62:65], v[86:89], v[180:183], v[62:65]
	v_mfma_i32_16x16x64_i8 v[58:61], v[94:97], v[180:183], v[58:61]
	v_mfma_i32_16x16x64_i8 v[46:49], v[86:89], v[188:191], v[46:49]
	v_mfma_i32_16x16x64_i8 v[42:45], v[94:97], v[188:191], v[42:45]
	v_mfma_i32_16x16x64_i8 v[30:33], v[86:89], v[196:199], v[30:33]
	v_mfma_i32_16x16x64_i8 v[26:29], v[94:97], v[196:199], v[26:29]
	v_mfma_i32_16x16x64_i8 v[14:17], v[86:89], v[204:207], v[14:17]
	v_mfma_i32_16x16x64_i8 v[10:13], v[94:97], v[204:207], v[10:13]
	s_setprio 0
	s_setprio 1
	v_mfma_i32_16x16x64_i8 v[54:57], v[160:163], v[176:179], v[54:57]
	v_mfma_i32_16x16x64_i8 v[50:53], v[168:171], v[176:179], v[50:53]
	v_mfma_i32_16x16x64_i8 v[38:41], v[160:163], v[184:187], v[38:41]
	v_mfma_i32_16x16x64_i8 v[34:37], v[168:171], v[184:187], v[34:37]
	v_mfma_i32_16x16x64_i8 v[22:25], v[160:163], v[192:195], v[22:25]
	v_mfma_i32_16x16x64_i8 v[18:21], v[168:171], v[192:195], v[18:21]
	v_mfma_i32_16x16x64_i8 v[6:9], v[160:163], v[200:203], v[6:9]
	v_mfma_i32_16x16x64_i8 v[2:5], v[168:171], v[200:203], v[2:5]
	v_mfma_i32_16x16x64_i8 v[54:57], v[164:167], v[180:183], v[54:57]
	v_mfma_i32_16x16x64_i8 v[50:53], v[172:175], v[180:183], v[50:53]
	v_mfma_i32_16x16x64_i8 v[38:41], v[164:167], v[188:191], v[38:41]
	v_mfma_i32_16x16x64_i8 v[34:37], v[172:175], v[188:191], v[34:37]
	v_mfma_i32_16x16x64_i8 v[22:25], v[164:167], v[196:199], v[22:25]
	v_mfma_i32_16x16x64_i8 v[18:21], v[172:175], v[196:199], v[18:21]
	v_mfma_i32_16x16x64_i8 v[6:9], v[164:167], v[204:207], v[6:9]
	v_mfma_i32_16x16x64_i8 v[2:5], v[172:175], v[204:207], v[2:5]
	s_setprio 0
	s_barrier
	s_add_i32 s70, 0, 0x18000
	v_add_u32_e32 v0, s70, v157
	s_add_i32 s71, 0, 0x1c000
	ds_read_b128 v[82:85], v0
	ds_read_b128 v[86:89], v0 offset:1024
	ds_read_b128 v[90:93], v0 offset:2048
	ds_read_b128 v[94:97], v0 offset:3072
	v_add_u32_e32 v0, s71, v157
	ds_read_b128 v[160:163], v0
	ds_read_b128 v[164:167], v0 offset:1024
	ds_read_b128 v[168:171], v0 offset:2048
	ds_read_b128 v[172:175], v0 offset:3072
	s_add_u32 s68, s42, 0x20000
	v_mov_b32_e32 v0, v149
	s_mov_b32 m0, s57
	ds_read_b128 v[176:179], v159 offset:32768
	ds_read_b128 v[180:183], v159 offset:33792
	ds_read_b128 v[184:187], v159 offset:34816
	ds_read_b128 v[188:191], v159 offset:35840
	ds_read_b128 v[192:195], v159 offset:36864
	ds_read_b128 v[196:199], v159 offset:37888
	ds_read_b128 v[200:203], v159 offset:38912
	ds_read_b128 v[204:207], v159 offset:39936
	s_addc_u32 s69, s43, 0
	s_nop 0
	global_load_lds_dwordx4 v0, s[68:69]
	v_mov_b32_e32 v0, v153
	s_mov_b32 m0, s58
	s_nop 0
	global_load_lds_dwordx4 v0, s[68:69]
	s_waitcnt vmcnt(8)
	s_waitcnt lgkmcnt(0)
	s_barrier
	s_setprio 1
	s_waitcnt lgkmcnt(0)
	v_mfma_i32_16x16x64_i8 v[142:145], v[82:85], v[176:179], v[142:145]
	v_mfma_i32_16x16x64_i8 v[134:137], v[90:93], v[176:179], v[134:137]
	v_mfma_i32_16x16x64_i8 v[126:129], v[82:85], v[184:187], v[126:129]
	v_mfma_i32_16x16x64_i8 v[122:125], v[90:93], v[184:187], v[122:125]
	v_mfma_i32_16x16x64_i8 v[110:113], v[82:85], v[192:195], v[110:113]
	v_mfma_i32_16x16x64_i8 v[106:109], v[90:93], v[192:195], v[106:109]
	v_mfma_i32_16x16x64_i8 v[78:81], v[82:85], v[200:203], v[78:81]
	v_mfma_i32_16x16x64_i8 v[74:77], v[90:93], v[200:203], v[74:77]
	v_mfma_i32_16x16x64_i8 v[142:145], v[86:89], v[180:183], v[142:145]
	v_mfma_i32_16x16x64_i8 v[134:137], v[94:97], v[180:183], v[134:137]
	v_mfma_i32_16x16x64_i8 v[126:129], v[86:89], v[188:191], v[126:129]
	v_mfma_i32_16x16x64_i8 v[122:125], v[94:97], v[188:191], v[122:125]
	v_mfma_i32_16x16x64_i8 v[110:113], v[86:89], v[196:199], v[110:113]
	v_mfma_i32_16x16x64_i8 v[106:109], v[94:97], v[196:199], v[106:109]
	v_mfma_i32_16x16x64_i8 v[78:81], v[86:89], v[204:207], v[78:81]
	v_mfma_i32_16x16x64_i8 v[74:77], v[94:97], v[204:207], v[74:77]
	s_setprio 0
	s_setprio 1
	v_mfma_i32_16x16x64_i8 v[138:141], v[160:163], v[176:179], v[138:141]
	v_mfma_i32_16x16x64_i8 v[130:133], v[168:171], v[176:179], v[130:133]
	v_mfma_i32_16x16x64_i8 v[118:121], v[160:163], v[184:187], v[118:121]
	v_mfma_i32_16x16x64_i8 v[114:117], v[168:171], v[184:187], v[114:117]
	v_mfma_i32_16x16x64_i8 v[102:105], v[160:163], v[192:195], v[102:105]
	v_mfma_i32_16x16x64_i8 v[98:101], v[168:171], v[192:195], v[98:101]
	v_mfma_i32_16x16x64_i8 v[70:73], v[160:163], v[200:203], v[70:73]
	v_mfma_i32_16x16x64_i8 v[66:69], v[168:171], v[200:203], v[66:69]
	v_mfma_i32_16x16x64_i8 v[138:141], v[164:167], v[180:183], v[138:141]
	v_mfma_i32_16x16x64_i8 v[130:133], v[172:175], v[180:183], v[130:133]
	v_mfma_i32_16x16x64_i8 v[118:121], v[164:167], v[188:191], v[118:121]
	v_mfma_i32_16x16x64_i8 v[114:117], v[172:175], v[188:191], v[114:117]
	v_mfma_i32_16x16x64_i8 v[102:105], v[164:167], v[196:199], v[102:105]
	v_mfma_i32_16x16x64_i8 v[98:101], v[172:175], v[196:199], v[98:101]
	v_mfma_i32_16x16x64_i8 v[70:73], v[164:167], v[204:207], v[70:73]
	v_mfma_i32_16x16x64_i8 v[66:69], v[172:175], v[204:207], v[66:69]
	s_setprio 0
	s_barrier
	v_mov_b32_e32 v0, v151
	ds_read_b128 v[176:179], v159 offset:49152
	ds_read_b128 v[180:183], v159 offset:50176
	ds_read_b128 v[184:187], v159 offset:51200
	ds_read_b128 v[188:191], v159 offset:52224
	ds_read_b128 v[192:195], v159 offset:53248
	ds_read_b128 v[196:199], v159 offset:54272
	ds_read_b128 v[200:203], v159 offset:55296
	ds_read_b128 v[204:207], v159 offset:56320
	s_add_i32 s68, s70, s33
	v_lshl_add_u64 v[146:147], s[44:45], 0, v[0:1]
	v_lshl_add_u64 v[146:147], v[146:147], 0, s[90:91]
	s_mov_b32 m0, s68
	v_mov_b32_e32 v0, v155
	global_load_lds_dwordx4 v[146:147], off
	s_add_i32 m0, s68, 0x2000
	s_nop 0
	v_lshl_add_u64 v[146:147], s[44:45], 0, v[0:1]
	s_add_u32 s44, s44, 0x20080
	v_lshl_add_u64 v[146:147], v[146:147], 0, s[90:91]
	s_addc_u32 s45, s45, 0
	v_mov_b32_e32 v0, v151
	s_add_i32 s68, s71, s33
	global_load_lds_dwordx4 v[146:147], off
	s_mov_b32 m0, s68
	s_nop 0
	global_load_lds_dwordx4 v0, s[44:45]
	v_mov_b32_e32 v0, v155
	s_add_i32 m0, s68, 0x2000
	s_nop 0
	global_load_lds_dwordx4 v0, s[44:45]
	v_mov_b32_e32 v0, v149
	s_mov_b32 m0, s61
	v_lshl_add_u64 v[146:147], s[42:43], 0, v[0:1]
	v_lshl_add_u64 v[146:147], v[146:147], 0, s[90:91]
	v_mov_b32_e32 v0, v153
	global_load_lds_dwordx4 v[146:147], off
	s_mov_b32 m0, s62
	v_lshl_add_u64 v[146:147], s[42:43], 0, v[0:1]
	v_lshl_add_u64 v[146:147], v[146:147], 0, s[90:91]
	global_load_lds_dwordx4 v[146:147], off
	s_waitcnt vmcnt(8)
	s_waitcnt lgkmcnt(0)
	s_barrier
	s_setprio 1
	s_waitcnt lgkmcnt(0)
	v_mfma_i32_16x16x64_i8 v[62:65], v[82:85], v[176:179], v[62:65]
	v_mfma_i32_16x16x64_i8 v[58:61], v[90:93], v[176:179], v[58:61]
	v_mfma_i32_16x16x64_i8 v[46:49], v[82:85], v[184:187], v[46:49]
	v_mfma_i32_16x16x64_i8 v[42:45], v[90:93], v[184:187], v[42:45]
	v_mfma_i32_16x16x64_i8 v[30:33], v[82:85], v[192:195], v[30:33]
	v_mfma_i32_16x16x64_i8 v[26:29], v[90:93], v[192:195], v[26:29]
	v_mfma_i32_16x16x64_i8 v[14:17], v[82:85], v[200:203], v[14:17]
	v_mfma_i32_16x16x64_i8 v[10:13], v[90:93], v[200:203], v[10:13]
	v_mfma_i32_16x16x64_i8 v[62:65], v[86:89], v[180:183], v[62:65]
	v_mfma_i32_16x16x64_i8 v[58:61], v[94:97], v[180:183], v[58:61]
	v_mfma_i32_16x16x64_i8 v[46:49], v[86:89], v[188:191], v[46:49]
	v_mfma_i32_16x16x64_i8 v[42:45], v[94:97], v[188:191], v[42:45]
	v_mfma_i32_16x16x64_i8 v[30:33], v[86:89], v[196:199], v[30:33]
	v_mfma_i32_16x16x64_i8 v[26:29], v[94:97], v[196:199], v[26:29]
	v_mfma_i32_16x16x64_i8 v[14:17], v[86:89], v[204:207], v[14:17]
	v_mfma_i32_16x16x64_i8 v[10:13], v[94:97], v[204:207], v[10:13]
	s_setprio 0
	s_setprio 1
	v_mfma_i32_16x16x64_i8 v[54:57], v[160:163], v[176:179], v[54:57]
	v_mfma_i32_16x16x64_i8 v[50:53], v[168:171], v[176:179], v[50:53]
	v_mfma_i32_16x16x64_i8 v[38:41], v[160:163], v[184:187], v[38:41]
	v_mfma_i32_16x16x64_i8 v[34:37], v[168:171], v[184:187], v[34:37]
	v_mfma_i32_16x16x64_i8 v[22:25], v[160:163], v[192:195], v[22:25]
	v_mfma_i32_16x16x64_i8 v[18:21], v[168:171], v[192:195], v[18:21]
	v_mfma_i32_16x16x64_i8 v[6:9], v[160:163], v[200:203], v[6:9]
	v_mfma_i32_16x16x64_i8 v[2:5], v[168:171], v[200:203], v[2:5]
	v_mfma_i32_16x16x64_i8 v[54:57], v[164:167], v[180:183], v[54:57]
	v_mfma_i32_16x16x64_i8 v[50:53], v[172:175], v[180:183], v[50:53]
	v_mfma_i32_16x16x64_i8 v[38:41], v[164:167], v[188:191], v[38:41]
	v_mfma_i32_16x16x64_i8 v[34:37], v[172:175], v[188:191], v[34:37]
	v_mfma_i32_16x16x64_i8 v[22:25], v[164:167], v[196:199], v[22:25]
	v_mfma_i32_16x16x64_i8 v[18:21], v[172:175], v[196:199], v[18:21]
	v_mfma_i32_16x16x64_i8 v[6:9], v[164:167], v[204:207], v[6:9]
	v_mfma_i32_16x16x64_i8 v[2:5], v[172:175], v[204:207], v[2:5]
	s_setprio 0
	s_barrier
	s_add_i32 s67, s67, 2
	s_add_u32 s40, s40, 0x100
	s_addc_u32 s41, s41, 0
	s_add_u32 s37, s37, 0x100
	s_addc_u32 s66, s66, 0
	s_cmp_gt_u32 s67, 5
	s_cbranch_scc0 .LBB0_1508
	s_lshl_b32 s23, s38, 8
	s_add_i32 s23, s23, s87
	s_mul_i32 s37, s65, 0x5800
	s_mul_hi_i32 s29, s65, 0x5800
	s_add_u32 s37, s59, s37
	s_addc_u32 s29, s60, s29
	s_lshl_b32 s40, s36, 8
	s_ashr_i32 s41, s40, 31
	s_lshl_b64 s[40:41], s[40:41], 2
	s_add_u32 s37, s37, s40
	v_mbcnt_lo_u32_b32 v0, -1, 0
	v_mbcnt_hi_u32_b32 v0, -1, v0
	s_addc_u32 s29, s29, s41
	v_lshrrev_b32_e32 v82, 1, v0
	s_lshl_b32 s38, s72, 2
	v_and_or_b32 v160, v0, 15, s23
	v_and_b32_e32 v162, 24, v82
	s_add_u32 s40, s37, s38
	v_ashrrev_i32_e32 v161, 31, v160
	s_addc_u32 s41, s29, 0
	v_lshlrev_b32_e32 v90, 2, v162
	v_lshl_add_u64 v[146:147], v[160:161], 2, s[20:21]
	global_load_dwordx4 v[86:89], v90, s[40:41] offset:16
	global_load_dwordx4 v[94:97], v90, s[40:41]
	global_load_dwordx4 v[82:85], v90, s[40:41] offset:528
	s_nop 0
	global_load_dwordx4 v[90:93], v90, s[40:41] offset:512
	v_cvt_f32_i32_e32 v173, v143
	global_load_dword v170, v[146:147], off
	global_load_dword v158, v[146:147], off offset:64
	global_load_dword v156, v[146:147], off offset:128
	global_load_dword v154, v[146:147], off offset:192
	global_load_dword v152, v[146:147], off offset:512
	global_load_dword v150, v[146:147], off offset:576
	global_load_dword v148, v[146:147], off offset:640
	global_load_dword v0, v[146:147], off offset:704
	v_cvt_f32_i32_e32 v172, v142
	v_cvt_f32_i32_e32 v143, v145
	v_cvt_f32_i32_e32 v142, v144
	s_lshl_b32 s23, s36, 7
	s_or_b32 s23, s23, s72
	v_or_b32_e32 v146, s23, v162
	v_cvt_f32_i32_e32 v133, v133
	v_cvt_f32_i32_e32 v132, v132
	v_cvt_f32_i32_e32 v131, v131
	v_cvt_f32_i32_e32 v130, v130
	s_mov_b32 s23, 0xc3e00000
	s_movk_i32 s29, 0xb00
	v_cvt_f32_i32_e32 v127, v127
	v_cvt_f32_i32_e32 v126, v126
	v_ashrrev_i32_e32 v147, 31, v146
	v_mov_b64_e32 v[176:177], s[18:19]
	v_mad_i64_i32 v[176:177], s[36:37], v160, s29, v[176:177]
	v_lshl_add_u64 v[176:177], v[176:177], 0, v[146:147]
	s_mov_b32 s41, 0
	s_mov_b32 s40, 0xb000
	v_lshl_add_u64 v[178:179], v[176:177], 0, s[40:41]
	s_mov_b32 s40, 0x16000
	v_lshl_add_u64 v[180:181], v[176:177], 0, s[40:41]
	s_mov_b32 s40, 0x21000
	v_lshl_add_u64 v[182:183], v[176:177], 0, s[40:41]
	s_mov_b32 s40, 0x58000
	v_lshl_add_u64 v[184:185], v[176:177], 0, s[40:41]
	s_mov_b32 s40, 0x63000
	v_lshl_add_u64 v[186:187], v[176:177], 0, s[40:41]
	s_mov_b32 s40, 0x6e000
	v_lshl_add_u64 v[188:189], v[176:177], 0, s[40:41]
	s_mov_b32 s40, 0x79000
	v_lshl_add_u64 v[190:191], v[176:177], 0, s[40:41]
	v_cvt_f32_i32_e32 v129, v129
	v_cvt_f32_i32_e32 v128, v128
	v_cvt_f32_i32_e32 v119, v119
	v_cvt_f32_i32_e32 v118, v118
	v_cvt_f32_i32_e32 v121, v121
	v_cvt_f32_i32_e32 v120, v120
	v_cvt_f32_i32_e32 v123, v123
	v_cvt_f32_i32_e32 v122, v122
	v_cvt_f32_i32_e32 v125, v125
	v_cvt_f32_i32_e32 v124, v124
	v_cvt_f32_i32_e32 v115, v115
	v_cvt_f32_i32_e32 v114, v114
	v_cvt_f32_i32_e32 v117, v117
	v_cvt_f32_i32_e32 v116, v116
	v_cvt_f32_i32_e32 v111, v111
	v_cvt_f32_i32_e32 v110, v110
	v_cvt_f32_i32_e32 v113, v113
	v_cvt_f32_i32_e32 v112, v112
	v_cvt_f32_i32_e32 v103, v103
	v_cvt_f32_i32_e32 v102, v102
	v_cvt_f32_i32_e32 v105, v105
	v_cvt_f32_i32_e32 v104, v104
	v_cvt_f32_i32_e32 v107, v107
	v_cvt_f32_i32_e32 v106, v106
	v_cvt_f32_i32_e32 v109, v109
	v_cvt_f32_i32_e32 v108, v108
	v_cvt_f32_i32_e32 v99, v99
	v_cvt_f32_i32_e32 v98, v98
	v_cvt_f32_i32_e32 v101, v101
	v_cvt_f32_i32_e32 v100, v100
	v_cvt_f32_i32_e32 v79, v79
	v_cvt_f32_i32_e32 v78, v78
	v_readlane_b32 s40, v254, 19
	v_readlane_b32 s41, v254, 20
	s_and_b64 vcc, exec, s[40:41]
	s_cbranch_vccz .LBB0_1511
	s_barrier
.LBB0_1511:
	v_cvt_f32_i32_e32 v81, v81
	v_cvt_f32_i32_e32 v80, v80
	v_cvt_f32_i32_e32 v71, v71
	v_cvt_f32_i32_e32 v70, v70
	v_cvt_f32_i32_e32 v73, v73
	v_cvt_f32_i32_e32 v72, v72
	v_cvt_f32_i32_e32 v75, v75
	v_cvt_f32_i32_e32 v74, v74
	v_cvt_f32_i32_e32 v77, v77
	v_cvt_f32_i32_e32 v76, v76
	v_cvt_f32_i32_e32 v67, v67
	v_cvt_f32_i32_e32 v66, v66
	v_cvt_f32_i32_e32 v69, v69
	v_cvt_f32_i32_e32 v68, v68
	v_cvt_f32_i32_e32 v63, v63
	v_cvt_f32_i32_e32 v62, v62
	v_cvt_f32_i32_e32 v65, v65
	v_cvt_f32_i32_e32 v64, v64
	v_cvt_f32_i32_e32 v55, v55
	v_cvt_f32_i32_e32 v54, v54
	v_cvt_f32_i32_e32 v57, v57
	v_cvt_f32_i32_e32 v56, v56
	v_cvt_f32_i32_e32 v59, v59
	v_cvt_f32_i32_e32 v58, v58
	v_cvt_f32_i32_e32 v61, v61
	v_cvt_f32_i32_e32 v60, v60
	v_cvt_f32_i32_e32 v51, v51
	v_cvt_f32_i32_e32 v50, v50
	v_cvt_f32_i32_e32 v53, v53
	v_cvt_f32_i32_e32 v52, v52
	v_cvt_f32_i32_e32 v47, v47
	v_cvt_f32_i32_e32 v46, v46
	v_cvt_f32_i32_e32 v49, v49
	v_cvt_f32_i32_e32 v48, v48
	v_cvt_f32_i32_e32 v39, v39
	v_cvt_f32_i32_e32 v38, v38
	v_cvt_f32_i32_e32 v41, v41
	v_cvt_f32_i32_e32 v40, v40
	v_cvt_f32_i32_e32 v43, v43
	v_cvt_f32_i32_e32 v42, v42
	v_cvt_f32_i32_e32 v45, v45
	v_cvt_f32_i32_e32 v44, v44
	v_cvt_f32_i32_e32 v35, v35
	v_cvt_f32_i32_e32 v34, v34
	v_cvt_f32_i32_e32 v37, v37
	v_cvt_f32_i32_e32 v36, v36
	v_cvt_f32_i32_e32 v31, v31
	v_cvt_f32_i32_e32 v30, v30
	v_cvt_f32_i32_e32 v33, v33
	v_cvt_f32_i32_e32 v32, v32
	v_cvt_f32_i32_e32 v23, v23
	v_cvt_f32_i32_e32 v22, v22
	v_cvt_f32_i32_e32 v25, v25
	v_cvt_f32_i32_e32 v24, v24
	v_cvt_f32_i32_e32 v27, v27
	v_cvt_f32_i32_e32 v26, v26
	v_cvt_f32_i32_e32 v29, v29
	v_cvt_f32_i32_e32 v28, v28
	v_cvt_f32_i32_e32 v19, v19
	v_cvt_f32_i32_e32 v18, v18
	v_cvt_f32_i32_e32 v21, v21
	v_cvt_f32_i32_e32 v20, v20
	v_cvt_f32_i32_e32 v17, v17
	v_cvt_f32_i32_e32 v16, v16
	v_cvt_f32_i32_e32 v15, v15
	v_cvt_f32_i32_e32 v14, v14
	v_cvt_f32_i32_e32 v9, v9
	v_cvt_f32_i32_e32 v8, v8
	v_cvt_f32_i32_e32 v7, v7
	v_cvt_f32_i32_e32 v6, v6
	v_cvt_f32_i32_e32 v13, v13
	v_cvt_f32_i32_e32 v12, v12
	v_cvt_f32_i32_e32 v3, v3
	v_cvt_f32_i32_e32 v2, v2
	v_cvt_f32_i32_e32 v11, v11
	v_cvt_f32_i32_e32 v10, v10
	v_cvt_f32_i32_e32 v5, v5
	v_cvt_f32_i32_e32 v4, v4
	s_waitcnt vmcnt(0)
	v_mul_f32_e32 v94, 0x3fb8aa3b, v94
	v_mul_f32_e32 v95, 0x3fb8aa3b, v95
	v_mul_f32_e32 v96, 0x3fb8aa3b, v96
	v_mul_f32_e32 v97, 0x3fb8aa3b, v97
	v_mul_f32_e32 v86, 0x3fb8aa3b, v86
	v_mul_f32_e32 v87, 0x3fb8aa3b, v87
	v_mul_f32_e32 v88, 0x3fb8aa3b, v88
	v_mul_f32_e32 v89, 0x3fb8aa3b, v89
	v_mul_f32_e32 v90, 0x3f317218, v90
	v_mul_f32_e32 v91, 0x3f317218, v91
	v_mul_f32_e32 v92, 0x3f317218, v92
	v_mul_f32_e32 v93, 0x3f317218, v93
	v_mul_f32_e32 v82, 0x3f317218, v82
	v_mul_f32_e32 v83, 0x3f317218, v83
	v_mul_f32_e32 v84, 0x3f317218, v84
	v_mul_f32_e32 v85, 0x3f317218, v85
	v_pk_mul_f32 v[144:145], v[96:97], v[170:171] op_sel_hi:[1,0]
	v_pk_mul_f32 v[174:175], v[94:95], v[170:171] op_sel_hi:[1,0]
	v_pk_mul_f32 v[142:143], v[144:145], v[142:143]
	v_pk_mul_f32 v[144:145], v[174:175], v[172:173]
	v_cvt_f32_i32_e32 v173, v139
	v_cvt_f32_i32_e32 v172, v138
	v_cvt_f32_i32_e32 v139, v141
	v_cvt_f32_i32_e32 v138, v140
	v_mul_f32_e32 v162, 4.0, v170
	v_pk_mul_f32 v[140:141], v[92:93], v[162:163] op_sel_hi:[1,0]
	v_pk_mul_f32 v[174:175], v[90:91], v[162:163] op_sel_hi:[1,0]
	v_pk_mul_f32 v[138:139], v[140:141], v[138:139]
	v_pk_mul_f32 v[140:141], v[174:175], v[172:173]
	v_cvt_f32_i32_e32 v173, v135
	v_cvt_f32_i32_e32 v172, v134
	v_cvt_f32_i32_e32 v135, v137
	v_cvt_f32_i32_e32 v134, v136
	v_pk_mul_f32 v[136:137], v[88:89], v[170:171] op_sel_hi:[1,0]
	v_pk_mul_f32 v[170:171], v[86:87], v[170:171] op_sel_hi:[1,0]
	v_pk_mul_f32 v[134:135], v[136:137], v[134:135]
	v_pk_mul_f32 v[136:137], v[170:171], v[172:173]
	v_pk_mul_f32 v[170:171], v[84:85], v[162:163] op_sel_hi:[1,0]
	v_pk_mul_f32 v[172:173], v[82:83], v[162:163] op_sel_hi:[1,0]
	v_pk_mul_f32 v[132:133], v[170:171], v[132:133]
	v_pk_mul_f32 v[130:131], v[172:173], v[130:131]
	v_exp_f32_e64 v162, -v144
	v_exp_f32_e64 v170, -v142
	v_exp_f32_e64 v169, -v145
	v_exp_f32_e64 v171, -v143
	v_exp_f32_e64 v172, -v136
	v_exp_f32_e64 v174, -v134
	v_exp_f32_e64 v173, -v137
	v_exp_f32_e64 v175, -v135
	v_add_f32_e32 v162, 1.0, v162
	v_add_f32_e32 v170, 1.0, v170
	v_rcp_f32_e32 v162, v162
	v_add_f32_e32 v169, 1.0, v169
	v_rcp_f32_e32 v170, v170
	v_add_f32_e32 v171, 1.0, v171
	v_add_f32_e32 v172, 1.0, v172
	v_add_f32_e32 v174, 1.0, v174
	v_rcp_f32_e32 v169, v169
	v_rcp_f32_e32 v171, v171
	v_rcp_f32_e32 v172, v172
	v_add_f32_e32 v173, 1.0, v173
	v_rcp_f32_e32 v174, v174
	v_add_f32_e32 v175, 1.0, v175
	v_rcp_f32_e32 v173, v173
	v_rcp_f32_e32 v175, v175
	v_mul_f32_e32 v144, v144, v162
	v_mul_f32_e32 v142, v142, v170
	v_mul_f32_e32 v140, v140, v144
	v_mul_f32_e32 v144, v145, v169
	v_mul_f32_e32 v138, v138, v142
	v_mul_f32_e32 v142, v143, v171
	v_mul_f32_e32 v136, v136, v172
	v_mul_f32_e32 v134, v134, v174
	v_mul_f32_e32 v141, v141, v144
	v_mul_f32_e32 v139, v139, v142
	v_mul_f32_e32 v130, v130, v136
	v_mul_f32_e32 v136, v137, v173
	v_mul_f32_e32 v134, v132, v134
	v_mul_f32_e32 v132, v135, v175
	v_mov_b32_e32 v142, 0x43e00000
	v_mul_f32_e32 v131, v131, v136
	v_mul_f32_e32 v133, v133, v132
	v_med3_f32 v135, v140, s23, v142
	v_med3_f32 v136, v141, s23, v142
	v_cvt_pk_fp8_f32 v132, v135, v136
	v_med3_f32 v130, v130, s23, v142
	v_med3_f32 v131, v131, s23, v142
	v_med3_f32 v135, v133, s23, v142
	v_cvt_pk_fp8_f32 v133, v130, v131
	v_med3_f32 v137, v138, s23, v142
	v_med3_f32 v138, v139, s23, v142
	v_med3_f32 v134, v134, s23, v142
	v_cvt_pk_fp8_f32 v132, v137, v138 op_sel:[0,0,1]
	v_cvt_pk_fp8_f32 v133, v134, v135 op_sel:[0,0,1]
	global_store_dwordx2 v[176:177], v[132:133], off
	v_mul_f32_e32 v132, 4.0, v158
	v_pk_mul_f32 v[136:137], v[94:95], v[158:159] op_sel_hi:[1,0]
	v_pk_mul_f32 v[134:135], v[96:97], v[158:159] op_sel_hi:[1,0]
	v_pk_mul_f32 v[126:127], v[136:137], v[126:127]
	v_pk_mul_f32 v[136:137], v[90:91], v[132:133] op_sel_hi:[1,0]
	v_pk_mul_f32 v[128:129], v[134:135], v[128:129]
	v_pk_mul_f32 v[134:135], v[92:93], v[132:133] op_sel_hi:[1,0]
	v_pk_mul_f32 v[118:119], v[136:137], v[118:119]
	v_pk_mul_f32 v[136:137], v[86:87], v[158:159] op_sel_hi:[1,0]
	v_pk_mul_f32 v[120:121], v[134:135], v[120:121]
	v_pk_mul_f32 v[134:135], v[88:89], v[158:159] op_sel_hi:[1,0]
	v_pk_mul_f32 v[122:123], v[136:137], v[122:123]
	v_pk_mul_f32 v[124:125], v[134:135], v[124:125]
	v_pk_mul_f32 v[134:135], v[84:85], v[132:133] op_sel_hi:[1,0]
	v_pk_mul_f32 v[132:133], v[82:83], v[132:133] op_sel_hi:[1,0]
	v_pk_mul_f32 v[114:115], v[132:133], v[114:115]
	v_exp_f32_e64 v136, -v122
	v_exp_f32_e64 v132, -v126
	v_exp_f32_e64 v137, -v123
	v_exp_f32_e64 v133, -v127
	v_exp_f32_e64 v138, -v124
	v_exp_f32_e64 v139, -v125
	v_add_f32_e32 v136, 1.0, v136
	v_pk_mul_f32 v[116:117], v[134:135], v[116:117]
	v_add_f32_e32 v132, 1.0, v132
	v_rcp_f32_e32 v136, v136
	v_add_f32_e32 v137, 1.0, v137
	v_exp_f32_e64 v134, -v128
	v_rcp_f32_e32 v132, v132
	v_add_f32_e32 v133, 1.0, v133
	v_rcp_f32_e32 v137, v137
	v_add_f32_e32 v138, 1.0, v138
	v_exp_f32_e64 v135, -v129
	v_rcp_f32_e32 v133, v133
	v_rcp_f32_e32 v138, v138
	v_add_f32_e32 v139, 1.0, v139
	v_rcp_f32_e32 v139, v139
	v_mul_f32_e32 v122, v122, v136
	v_add_f32_e32 v134, 1.0, v134
	v_mul_f32_e32 v126, v126, v132
	v_mul_f32_e32 v122, v114, v122
	v_mul_f32_e32 v114, v123, v137
	v_rcp_f32_e32 v134, v134
	v_add_f32_e32 v135, 1.0, v135
	v_mul_f32_e32 v118, v118, v126
	v_mul_f32_e32 v126, v127, v133
	v_mul_f32_e32 v115, v115, v114
	v_mul_f32_e32 v114, v124, v138
	v_rcp_f32_e32 v135, v135
	v_mul_f32_e32 v119, v119, v126
	v_mul_f32_e32 v116, v116, v114
	v_mul_f32_e32 v114, v125, v139
	v_mul_f32_e32 v117, v117, v114
	v_med3_f32 v118, v118, s23, v142
	v_med3_f32 v119, v119, s23, v142
	v_cvt_pk_fp8_f32 v114, v118, v119
	v_med3_f32 v118, v122, s23, v142
	v_med3_f32 v119, v115, s23, v142
	v_mul_f32_e32 v126, v128, v134
	v_cvt_pk_fp8_f32 v115, v118, v119
	v_mul_f32_e32 v120, v120, v126
	v_mul_f32_e32 v126, v129, v135
	v_mul_f32_e32 v121, v121, v126
	v_med3_f32 v120, v120, s23, v142
	v_med3_f32 v121, v121, s23, v142
	v_med3_f32 v116, v116, s23, v142
	v_med3_f32 v117, v117, s23, v142
	v_cvt_pk_fp8_f32 v114, v120, v121 op_sel:[0,0,1]
	v_cvt_pk_fp8_f32 v115, v116, v117 op_sel:[0,0,1]
	global_store_dwordx2 v[178:179], v[114:115], off
	v_mul_f32_e32 v114, 4.0, v156
	v_pk_mul_f32 v[118:119], v[94:95], v[156:157] op_sel_hi:[1,0]
	v_pk_mul_f32 v[116:117], v[96:97], v[156:157] op_sel_hi:[1,0]
	v_pk_mul_f32 v[110:111], v[118:119], v[110:111]
	v_pk_mul_f32 v[118:119], v[90:91], v[114:115] op_sel_hi:[1,0]
	v_pk_mul_f32 v[112:113], v[116:117], v[112:113]
	v_pk_mul_f32 v[116:117], v[92:93], v[114:115] op_sel_hi:[1,0]
	v_pk_mul_f32 v[102:103], v[118:119], v[102:103]
	v_pk_mul_f32 v[118:119], v[86:87], v[156:157] op_sel_hi:[1,0]
	v_pk_mul_f32 v[104:105], v[116:117], v[104:105]
	v_pk_mul_f32 v[116:117], v[88:89], v[156:157] op_sel_hi:[1,0]
	v_pk_mul_f32 v[106:107], v[118:119], v[106:107]
	v_pk_mul_f32 v[108:109], v[116:117], v[108:109]
	v_pk_mul_f32 v[116:117], v[84:85], v[114:115] op_sel_hi:[1,0]
	v_pk_mul_f32 v[114:115], v[82:83], v[114:115] op_sel_hi:[1,0]
	v_pk_mul_f32 v[98:99], v[114:115], v[98:99]
	v_exp_f32_e64 v118, -v106
	v_exp_f32_e64 v114, -v110
	v_exp_f32_e64 v119, -v107
	v_exp_f32_e64 v115, -v111
	v_exp_f32_e64 v120, -v108
	v_exp_f32_e64 v121, -v109
	v_add_f32_e32 v118, 1.0, v118
	v_pk_mul_f32 v[100:101], v[116:117], v[100:101]
	v_add_f32_e32 v114, 1.0, v114
	v_rcp_f32_e32 v118, v118
	v_add_f32_e32 v119, 1.0, v119
	v_exp_f32_e64 v116, -v112
	v_rcp_f32_e32 v114, v114
	v_add_f32_e32 v115, 1.0, v115
	v_rcp_f32_e32 v119, v119
	v_add_f32_e32 v120, 1.0, v120
	v_exp_f32_e64 v117, -v113
	v_rcp_f32_e32 v115, v115
	v_rcp_f32_e32 v120, v120
	v_add_f32_e32 v121, 1.0, v121
	v_rcp_f32_e32 v121, v121
	v_mul_f32_e32 v106, v106, v118
	v_add_f32_e32 v116, 1.0, v116
	v_mul_f32_e32 v110, v110, v114
	v_mul_f32_e32 v106, v98, v106
	v_mul_f32_e32 v98, v107, v119
	v_rcp_f32_e32 v116, v116
	v_add_f32_e32 v117, 1.0, v117
	v_mul_f32_e32 v102, v102, v110
	v_mul_f32_e32 v110, v111, v115
	v_mul_f32_e32 v99, v99, v98
	v_mul_f32_e32 v98, v108, v120
	v_rcp_f32_e32 v117, v117
	v_mul_f32_e32 v103, v103, v110
	v_mul_f32_e32 v100, v100, v98
	v_mul_f32_e32 v98, v109, v121
	v_mul_f32_e32 v101, v101, v98
	v_med3_f32 v102, v102, s23, v142
	v_med3_f32 v103, v103, s23, v142
	v_cvt_pk_fp8_f32 v98, v102, v103
	v_med3_f32 v102, v106, s23, v142
	v_med3_f32 v103, v99, s23, v142
	v_mul_f32_e32 v110, v112, v116
	v_cvt_pk_fp8_f32 v99, v102, v103
	v_mul_f32_e32 v104, v104, v110
	v_mul_f32_e32 v110, v113, v117
	v_mul_f32_e32 v105, v105, v110
	v_med3_f32 v104, v104, s23, v142
	v_med3_f32 v105, v105, s23, v142
	v_med3_f32 v100, v100, s23, v142
	v_med3_f32 v101, v101, s23, v142
	v_cvt_pk_fp8_f32 v98, v104, v105 op_sel:[0,0,1]
	v_cvt_pk_fp8_f32 v99, v100, v101 op_sel:[0,0,1]
	global_store_dwordx2 v[180:181], v[98:99], off
	v_mul_f32_e32 v98, 4.0, v154
	v_pk_mul_f32 v[102:103], v[94:95], v[154:155] op_sel_hi:[1,0]
	v_pk_mul_f32 v[100:101], v[96:97], v[154:155] op_sel_hi:[1,0]
	v_pk_mul_f32 v[78:79], v[102:103], v[78:79]
	v_pk_mul_f32 v[102:103], v[90:91], v[98:99] op_sel_hi:[1,0]
	v_pk_mul_f32 v[80:81], v[100:101], v[80:81]
	v_pk_mul_f32 v[100:101], v[92:93], v[98:99] op_sel_hi:[1,0]
	v_pk_mul_f32 v[70:71], v[102:103], v[70:71]
	v_pk_mul_f32 v[102:103], v[86:87], v[154:155] op_sel_hi:[1,0]
	v_pk_mul_f32 v[72:73], v[100:101], v[72:73]
	v_pk_mul_f32 v[100:101], v[88:89], v[154:155] op_sel_hi:[1,0]
	v_pk_mul_f32 v[74:75], v[102:103], v[74:75]
	v_pk_mul_f32 v[76:77], v[100:101], v[76:77]
	v_pk_mul_f32 v[100:101], v[84:85], v[98:99] op_sel_hi:[1,0]
	v_pk_mul_f32 v[98:99], v[82:83], v[98:99] op_sel_hi:[1,0]
	v_pk_mul_f32 v[66:67], v[98:99], v[66:67]
	v_exp_f32_e64 v102, -v74
	v_exp_f32_e64 v98, -v78
	v_exp_f32_e64 v103, -v75
	v_exp_f32_e64 v99, -v79
	v_exp_f32_e64 v104, -v76
	v_exp_f32_e64 v105, -v77
	v_add_f32_e32 v102, 1.0, v102
	v_pk_mul_f32 v[68:69], v[100:101], v[68:69]
	v_add_f32_e32 v98, 1.0, v98
	v_rcp_f32_e32 v102, v102
	v_add_f32_e32 v103, 1.0, v103
	v_exp_f32_e64 v100, -v80
	v_rcp_f32_e32 v98, v98
	v_add_f32_e32 v99, 1.0, v99
	v_rcp_f32_e32 v103, v103
	v_add_f32_e32 v104, 1.0, v104
	v_exp_f32_e64 v101, -v81
	v_rcp_f32_e32 v99, v99
	v_rcp_f32_e32 v104, v104
	v_add_f32_e32 v105, 1.0, v105
	v_rcp_f32_e32 v105, v105
	v_mul_f32_e32 v74, v74, v102
	v_add_f32_e32 v100, 1.0, v100
	v_mul_f32_e32 v78, v78, v98
	v_mul_f32_e32 v74, v66, v74
	v_mul_f32_e32 v66, v75, v103
	v_rcp_f32_e32 v100, v100
	v_add_f32_e32 v101, 1.0, v101
	v_mul_f32_e32 v70, v70, v78
	v_mul_f32_e32 v78, v79, v99
	v_mul_f32_e32 v67, v67, v66
	v_mul_f32_e32 v66, v76, v104
	v_rcp_f32_e32 v101, v101
	v_mul_f32_e32 v71, v71, v78
	v_mul_f32_e32 v68, v68, v66
	v_mul_f32_e32 v66, v77, v105
	v_mul_f32_e32 v69, v69, v66
	v_med3_f32 v70, v70, s23, v142
	v_med3_f32 v71, v71, s23, v142
	v_cvt_pk_fp8_f32 v66, v70, v71
	v_med3_f32 v70, v74, s23, v142
	v_med3_f32 v71, v67, s23, v142
	v_mul_f32_e32 v78, v80, v100
	v_cvt_pk_fp8_f32 v67, v70, v71
	v_mul_f32_e32 v72, v72, v78
	v_mul_f32_e32 v78, v81, v101
	v_mul_f32_e32 v73, v73, v78
	v_med3_f32 v72, v72, s23, v142
	v_med3_f32 v73, v73, s23, v142
	v_med3_f32 v68, v68, s23, v142
	v_med3_f32 v69, v69, s23, v142
	v_cvt_pk_fp8_f32 v66, v72, v73 op_sel:[0,0,1]
	v_cvt_pk_fp8_f32 v67, v68, v69 op_sel:[0,0,1]
	global_store_dwordx2 v[182:183], v[66:67], off
	v_mul_f32_e32 v66, 4.0, v152
	v_pk_mul_f32 v[70:71], v[94:95], v[152:153] op_sel_hi:[1,0]
	v_pk_mul_f32 v[68:69], v[96:97], v[152:153] op_sel_hi:[1,0]
	v_pk_mul_f32 v[62:63], v[70:71], v[62:63]
	v_pk_mul_f32 v[70:71], v[90:91], v[66:67] op_sel_hi:[1,0]
	v_pk_mul_f32 v[64:65], v[68:69], v[64:65]
	v_pk_mul_f32 v[68:69], v[92:93], v[66:67] op_sel_hi:[1,0]
	v_pk_mul_f32 v[54:55], v[70:71], v[54:55]
	v_pk_mul_f32 v[70:71], v[86:87], v[152:153] op_sel_hi:[1,0]
	v_pk_mul_f32 v[56:57], v[68:69], v[56:57]
	v_pk_mul_f32 v[68:69], v[88:89], v[152:153] op_sel_hi:[1,0]
	v_pk_mul_f32 v[58:59], v[70:71], v[58:59]
	v_pk_mul_f32 v[60:61], v[68:69], v[60:61]
	v_pk_mul_f32 v[68:69], v[84:85], v[66:67] op_sel_hi:[1,0]
	v_pk_mul_f32 v[66:67], v[82:83], v[66:67] op_sel_hi:[1,0]
	v_pk_mul_f32 v[50:51], v[66:67], v[50:51]
	v_exp_f32_e64 v70, -v58
	v_exp_f32_e64 v66, -v62
	v_exp_f32_e64 v71, -v59
	v_exp_f32_e64 v67, -v63
	v_exp_f32_e64 v72, -v60
	v_exp_f32_e64 v73, -v61
	v_add_f32_e32 v70, 1.0, v70
	v_pk_mul_f32 v[52:53], v[68:69], v[52:53]
	v_add_f32_e32 v66, 1.0, v66
	v_rcp_f32_e32 v70, v70
	v_add_f32_e32 v71, 1.0, v71
	v_exp_f32_e64 v68, -v64
	v_rcp_f32_e32 v66, v66
	v_add_f32_e32 v67, 1.0, v67
	v_rcp_f32_e32 v71, v71
	v_add_f32_e32 v72, 1.0, v72
	v_exp_f32_e64 v69, -v65
	v_rcp_f32_e32 v67, v67
	v_rcp_f32_e32 v72, v72
	v_add_f32_e32 v73, 1.0, v73
	v_rcp_f32_e32 v73, v73
	v_mul_f32_e32 v58, v58, v70
	v_add_f32_e32 v68, 1.0, v68
	v_mul_f32_e32 v62, v62, v66
	v_mul_f32_e32 v58, v50, v58
	v_mul_f32_e32 v50, v59, v71
	v_rcp_f32_e32 v68, v68
	v_add_f32_e32 v69, 1.0, v69
	v_mul_f32_e32 v54, v54, v62
	v_mul_f32_e32 v62, v63, v67
	v_mul_f32_e32 v51, v51, v50
	v_mul_f32_e32 v50, v60, v72
	v_rcp_f32_e32 v69, v69
	v_mul_f32_e32 v55, v55, v62
	v_mul_f32_e32 v52, v52, v50
	v_mul_f32_e32 v50, v61, v73
	v_mul_f32_e32 v53, v53, v50
	v_med3_f32 v54, v54, s23, v142
	v_med3_f32 v55, v55, s23, v142
	v_cvt_pk_fp8_f32 v50, v54, v55
	v_med3_f32 v54, v58, s23, v142
	v_med3_f32 v55, v51, s23, v142
	v_mul_f32_e32 v62, v64, v68
	v_cvt_pk_fp8_f32 v51, v54, v55
	v_mul_f32_e32 v56, v56, v62
	v_mul_f32_e32 v62, v65, v69
	v_mul_f32_e32 v57, v57, v62
	v_med3_f32 v56, v56, s23, v142
	v_med3_f32 v57, v57, s23, v142
	v_med3_f32 v52, v52, s23, v142
	v_med3_f32 v53, v53, s23, v142
	v_cvt_pk_fp8_f32 v50, v56, v57 op_sel:[0,0,1]
	v_cvt_pk_fp8_f32 v51, v52, v53 op_sel:[0,0,1]
	global_store_dwordx2 v[184:185], v[50:51], off
	v_mul_f32_e32 v50, 4.0, v150
	v_pk_mul_f32 v[54:55], v[94:95], v[150:151] op_sel_hi:[1,0]
	v_pk_mul_f32 v[52:53], v[96:97], v[150:151] op_sel_hi:[1,0]
	v_pk_mul_f32 v[46:47], v[54:55], v[46:47]
	v_pk_mul_f32 v[54:55], v[90:91], v[50:51] op_sel_hi:[1,0]
	v_pk_mul_f32 v[48:49], v[52:53], v[48:49]
	v_pk_mul_f32 v[52:53], v[92:93], v[50:51] op_sel_hi:[1,0]
	v_pk_mul_f32 v[38:39], v[54:55], v[38:39]
	v_pk_mul_f32 v[54:55], v[86:87], v[150:151] op_sel_hi:[1,0]
	v_pk_mul_f32 v[40:41], v[52:53], v[40:41]
	v_pk_mul_f32 v[52:53], v[88:89], v[150:151] op_sel_hi:[1,0]
	v_pk_mul_f32 v[42:43], v[54:55], v[42:43]
	v_pk_mul_f32 v[44:45], v[52:53], v[44:45]
	v_pk_mul_f32 v[52:53], v[84:85], v[50:51] op_sel_hi:[1,0]
	v_pk_mul_f32 v[50:51], v[82:83], v[50:51] op_sel_hi:[1,0]
	v_pk_mul_f32 v[34:35], v[50:51], v[34:35]
	v_exp_f32_e64 v54, -v42
	v_exp_f32_e64 v50, -v46
	v_exp_f32_e64 v55, -v43
	v_exp_f32_e64 v51, -v47
	v_exp_f32_e64 v56, -v44
	v_exp_f32_e64 v57, -v45
	v_add_f32_e32 v54, 1.0, v54
	v_pk_mul_f32 v[36:37], v[52:53], v[36:37]
	v_add_f32_e32 v50, 1.0, v50
	v_rcp_f32_e32 v54, v54
	v_add_f32_e32 v55, 1.0, v55
	v_exp_f32_e64 v52, -v48
	v_rcp_f32_e32 v50, v50
	v_add_f32_e32 v51, 1.0, v51
	v_rcp_f32_e32 v55, v55
	v_add_f32_e32 v56, 1.0, v56
	v_exp_f32_e64 v53, -v49
	v_rcp_f32_e32 v51, v51
	v_rcp_f32_e32 v56, v56
	v_add_f32_e32 v57, 1.0, v57
	v_rcp_f32_e32 v57, v57
	v_mul_f32_e32 v42, v42, v54
	v_add_f32_e32 v52, 1.0, v52
	v_mul_f32_e32 v46, v46, v50
	v_mul_f32_e32 v42, v34, v42
	v_mul_f32_e32 v34, v43, v55
	v_rcp_f32_e32 v52, v52
	v_add_f32_e32 v53, 1.0, v53
	v_mul_f32_e32 v38, v38, v46
	v_mul_f32_e32 v46, v47, v51
	v_mul_f32_e32 v35, v35, v34
	v_mul_f32_e32 v34, v44, v56
	v_rcp_f32_e32 v53, v53
	v_mul_f32_e32 v39, v39, v46
	v_mul_f32_e32 v36, v36, v34
	v_mul_f32_e32 v34, v45, v57
	v_mul_f32_e32 v37, v37, v34
	v_med3_f32 v38, v38, s23, v142
	v_med3_f32 v39, v39, s23, v142
	v_cvt_pk_fp8_f32 v34, v38, v39
	v_med3_f32 v38, v42, s23, v142
	v_med3_f32 v39, v35, s23, v142
	v_mul_f32_e32 v46, v48, v52
	v_cvt_pk_fp8_f32 v35, v38, v39
	v_mul_f32_e32 v40, v40, v46
	v_mul_f32_e32 v46, v49, v53
	v_mul_f32_e32 v41, v41, v46
	v_med3_f32 v40, v40, s23, v142
	v_med3_f32 v41, v41, s23, v142
	v_med3_f32 v36, v36, s23, v142
	v_med3_f32 v37, v37, s23, v142
	v_cvt_pk_fp8_f32 v34, v40, v41 op_sel:[0,0,1]
	v_cvt_pk_fp8_f32 v35, v36, v37 op_sel:[0,0,1]
	global_store_dwordx2 v[186:187], v[34:35], off
	v_mul_f32_e32 v34, 4.0, v148
	v_pk_mul_f32 v[38:39], v[94:95], v[148:149] op_sel_hi:[1,0]
	v_pk_mul_f32 v[36:37], v[96:97], v[148:149] op_sel_hi:[1,0]
	v_pk_mul_f32 v[30:31], v[38:39], v[30:31]
	v_pk_mul_f32 v[38:39], v[90:91], v[34:35] op_sel_hi:[1,0]
	v_pk_mul_f32 v[32:33], v[36:37], v[32:33]
	v_pk_mul_f32 v[36:37], v[92:93], v[34:35] op_sel_hi:[1,0]
	v_pk_mul_f32 v[22:23], v[38:39], v[22:23]
	v_pk_mul_f32 v[38:39], v[86:87], v[148:149] op_sel_hi:[1,0]
	v_pk_mul_f32 v[24:25], v[36:37], v[24:25]
	v_pk_mul_f32 v[36:37], v[88:89], v[148:149] op_sel_hi:[1,0]
	v_pk_mul_f32 v[26:27], v[38:39], v[26:27]
	v_pk_mul_f32 v[28:29], v[36:37], v[28:29]
	v_pk_mul_f32 v[36:37], v[84:85], v[34:35] op_sel_hi:[1,0]
	v_pk_mul_f32 v[34:35], v[82:83], v[34:35] op_sel_hi:[1,0]
	v_pk_mul_f32 v[18:19], v[34:35], v[18:19]
	v_exp_f32_e64 v38, -v26
	v_exp_f32_e64 v34, -v30
	v_exp_f32_e64 v39, -v27
	v_exp_f32_e64 v35, -v31
	v_exp_f32_e64 v40, -v28
	v_exp_f32_e64 v41, -v29
	v_add_f32_e32 v38, 1.0, v38
	v_pk_mul_f32 v[20:21], v[36:37], v[20:21]
	v_add_f32_e32 v34, 1.0, v34
	v_rcp_f32_e32 v38, v38
	v_add_f32_e32 v39, 1.0, v39
	v_exp_f32_e64 v36, -v32
	v_rcp_f32_e32 v34, v34
	v_add_f32_e32 v35, 1.0, v35
	v_rcp_f32_e32 v39, v39
	v_add_f32_e32 v40, 1.0, v40
	v_exp_f32_e64 v37, -v33
	v_rcp_f32_e32 v35, v35
	v_rcp_f32_e32 v40, v40
	v_add_f32_e32 v41, 1.0, v41
	v_rcp_f32_e32 v41, v41
	v_mul_f32_e32 v26, v26, v38
	v_add_f32_e32 v36, 1.0, v36
	v_mul_f32_e32 v30, v30, v34
	v_mul_f32_e32 v26, v18, v26
	v_mul_f32_e32 v18, v27, v39
	v_rcp_f32_e32 v36, v36
	v_add_f32_e32 v37, 1.0, v37
	v_mul_f32_e32 v22, v22, v30
	v_mul_f32_e32 v30, v31, v35
	v_mul_f32_e32 v19, v19, v18
	v_mul_f32_e32 v18, v28, v40
	v_rcp_f32_e32 v37, v37
	v_mul_f32_e32 v23, v23, v30
	v_mul_f32_e32 v20, v20, v18
	v_mul_f32_e32 v18, v29, v41
	v_mul_f32_e32 v21, v21, v18
	v_med3_f32 v22, v22, s23, v142
	v_med3_f32 v23, v23, s23, v142
	v_cvt_pk_fp8_f32 v18, v22, v23
	v_med3_f32 v22, v26, s23, v142
	v_med3_f32 v23, v19, s23, v142
	v_mul_f32_e32 v30, v32, v36
	v_cvt_pk_fp8_f32 v19, v22, v23
	v_mul_f32_e32 v24, v24, v30
	v_mul_f32_e32 v30, v33, v37
	v_mul_f32_e32 v25, v25, v30
	v_med3_f32 v24, v24, s23, v142
	v_med3_f32 v25, v25, s23, v142
	v_med3_f32 v20, v20, s23, v142
	v_med3_f32 v21, v21, s23, v142
	v_cvt_pk_fp8_f32 v18, v24, v25 op_sel:[0,0,1]
	v_cvt_pk_fp8_f32 v19, v20, v21 op_sel:[0,0,1]
	global_store_dwordx2 v[188:189], v[18:19], off
	v_mul_f32_e32 v18, 4.0, v0
	v_pk_mul_f32 v[20:21], v[96:97], v[0:1] op_sel_hi:[1,0]
	v_pk_mul_f32 v[22:23], v[94:95], v[0:1] op_sel_hi:[1,0]
	v_pk_mul_f32 v[16:17], v[20:21], v[16:17]
	v_pk_mul_f32 v[20:21], v[92:93], v[18:19] op_sel_hi:[1,0]
	v_pk_mul_f32 v[14:15], v[22:23], v[14:15]
	v_pk_mul_f32 v[22:23], v[90:91], v[18:19] op_sel_hi:[1,0]
	v_pk_mul_f32 v[8:9], v[20:21], v[8:9]
	v_pk_mul_f32 v[20:21], v[88:89], v[0:1] op_sel_hi:[1,0]
	v_pk_mul_f32 v[6:7], v[22:23], v[6:7]
	v_pk_mul_f32 v[22:23], v[86:87], v[0:1] op_sel_hi:[1,0]
	v_pk_mul_f32 v[12:13], v[20:21], v[12:13]
	v_pk_mul_f32 v[20:21], v[84:85], v[18:19] op_sel_hi:[1,0]
	v_pk_mul_f32 v[18:19], v[82:83], v[18:19] op_sel_hi:[1,0]
	v_pk_mul_f32 v[2:3], v[18:19], v[2:3]
	v_exp_f32_e64 v0, -v14
	v_exp_f32_e64 v18, -v15
	v_pk_mul_f32 v[10:11], v[22:23], v[10:11]
	v_pk_mul_f32 v[4:5], v[20:21], v[4:5]
	v_exp_f32_e64 v19, -v16
	v_exp_f32_e64 v20, -v17
	v_exp_f32_e64 v21, -v10
	v_add_f32_e32 v0, 1.0, v0
	v_exp_f32_e64 v22, -v11
	v_rcp_f32_e32 v0, v0
	v_add_f32_e32 v18, 1.0, v18
	v_exp_f32_e64 v23, -v12
	v_rcp_f32_e32 v18, v18
	v_add_f32_e32 v19, 1.0, v19
	v_exp_f32_e64 v24, -v13
	v_rcp_f32_e32 v19, v19
	v_add_f32_e32 v20, 1.0, v20
	v_rcp_f32_e32 v20, v20
	v_add_f32_e32 v21, 1.0, v21
	v_rcp_f32_e32 v21, v21
	v_add_f32_e32 v22, 1.0, v22
	v_mul_f32_e32 v0, v14, v0
	v_rcp_f32_e32 v22, v22
	v_add_f32_e32 v23, 1.0, v23
	v_mul_f32_e32 v0, v6, v0
	v_mul_f32_e32 v6, v15, v18
	v_rcp_f32_e32 v23, v23
	v_add_f32_e32 v24, 1.0, v24
	v_mul_f32_e32 v6, v7, v6
	v_mul_f32_e32 v7, v16, v19
	v_rcp_f32_e32 v24, v24
	v_mul_f32_e32 v7, v8, v7
	v_mul_f32_e32 v8, v17, v20
	v_mul_f32_e32 v8, v9, v8
	v_mul_f32_e32 v9, v10, v21
	v_mul_f32_e32 v9, v2, v9
	v_mul_f32_e32 v2, v11, v22
	v_mul_f32_e32 v3, v3, v2
	v_mul_f32_e32 v2, v12, v23
	v_mul_f32_e32 v4, v4, v2
	v_mul_f32_e32 v2, v13, v24
	v_mul_f32_e32 v5, v5, v2
	v_med3_f32 v0, v0, s23, v142
	v_med3_f32 v6, v6, s23, v142
	v_cvt_pk_fp8_f32 v2, v0, v6
	v_med3_f32 v0, v9, s23, v142
	v_med3_f32 v6, v3, s23, v142
	v_cvt_pk_fp8_f32 v3, v0, v6
	v_med3_f32 v7, v7, s23, v142
	v_med3_f32 v8, v8, s23, v142
	v_med3_f32 v4, v4, s23, v142
	v_med3_f32 v5, v5, s23, v142
	v_cvt_pk_fp8_f32 v2, v7, v8 op_sel:[0,0,1]
	v_cvt_pk_fp8_f32 v3, v4, v5 op_sel:[0,0,1]
	s_mov_b64 s[36:37], -1
	s_and_b64 vcc, exec, s[8:9]
	global_store_dwordx2 v[190:191], v[2:3], off
	s_cbranch_vccnz .LBB0_1491
	s_and_b64 vcc, exec, s[6:7]
	s_cbranch_vccnz .LBB0_1490
	s_barrier
	s_branch .LBB0_1490
